# speedup vs baseline: 1.0421x; 1.0144x over previous
.LBB1_6:
	s_or_b64 exec, exec, s[12:13]
	s_load_dwordx4 s[36:39], s[0:1], 0x38
	s_add_i32 s0, 0, 0x23000
	v_lshl_add_u32 v222, v0, 2, s0
	v_readfirstlane_b32 s0, v0
	s_lshl_b32 s12, s0, 4
	s_and_b32 s0, s12, 0xfffffc00
	s_add_i32 s3, 0, 0x8000
	s_cmp_lg_u32 s3, -1
	s_cselect_b32 s1, s3, 0
	s_add_i32 s14, s0, s1
	s_add_u32 s0, s44, 0x2000
	v_mov_b32_e32 v2, 0x3c00
	v_cmp_eq_u32_e32 vcc, v221, v217
	v_or_b32_e32 v5, 1, v217
	v_lshlrev_b32_e32 v226, 4, v0
	s_mov_b32 m0, s14
	s_nop 0
	global_load_lds_dwordx4 v226, s[44:45]
	s_addc_u32 s1, s45, 0
	s_add_i32 s15, s14, 0x2000
	v_cndmask_b32_e32 v3, 0, v2, vcc
	v_or_b32_e32 v4, 2, v217
	v_cmp_eq_u32_e32 vcc, v221, v5
	s_mov_b32 m0, s15
	s_nop 0
	global_load_lds_dwordx4 v226, s[0:1]
	s_add_u32 s0, s44, 0x4000
	v_or_b32_e32 v7, 3, v217
	v_cndmask_b32_e32 v5, 0, v2, vcc
	v_cmp_eq_u32_e32 vcc, v221, v4
	s_addc_u32 s1, s45, 0
	s_add_i32 s15, s14, 0x4000
	v_cndmask_b32_e32 v4, 0, v2, vcc
	v_or_b32_e32 v6, 8, v217
	v_cmp_eq_u32_e32 vcc, v221, v7
	s_mov_b32 m0, s15
	s_nop 0
	global_load_lds_dwordx4 v226, s[0:1]
	s_add_u32 s0, s44, 0x6000
	v_or_b32_e32 v8, 10, v217
	v_cndmask_b32_e32 v7, 0, v2, vcc
	v_cmp_eq_u32_e32 vcc, v221, v6
	s_addc_u32 s1, s45, 0
	s_add_i32 s15, s14, 0x6000
	v_cndmask_b32_e32 v6, 0, v2, vcc
	v_or_b32_e32 v9, 9, v217
	v_cmp_eq_u32_e32 vcc, v221, v8
	s_mov_b32 m0, s15
	s_nop 0
	global_load_lds_dwordx4 v226, s[0:1]
	s_add_u32 s0, s44, 0x8000
	v_or_b32_e32 v10, 11, v217
	v_cndmask_b32_e32 v8, 0, v2, vcc
	v_cmp_eq_u32_e32 vcc, v221, v9
	s_addc_u32 s1, s45, 0
	s_and_b32 s12, s12, 0xfffff000
	v_cndmask_b32_e32 v9, 0, v2, vcc
	v_cmp_eq_u32_e32 vcc, v221, v10
	v_pack_b32_f16 v178, v3, v5
	v_or_b32_e32 v3, 16, v217
	s_sub_i32 s15, s14, s12
	v_cndmask_b32_e32 v10, 0, v2, vcc
	v_cmp_eq_u32_e32 vcc, v221, v3
	v_or_b32_e32 v5, 17, v217
	s_add_i32 s15, s15, 0x8000
	v_pack_b32_f16 v179, v4, v7
	v_cndmask_b32_e32 v3, 0, v2, vcc
	v_or_b32_e32 v4, 18, v217
	v_cmp_eq_u32_e32 vcc, v221, v5
	v_and_b32_e32 v224, 0xff0, v226
	s_mov_b32 m0, s15
	s_nop 0
	global_load_lds_dwordx4 v224, s[0:1]
	s_add_u32 s0, s44, 0x9000
	v_cndmask_b32_e32 v5, 0, v2, vcc
	v_cmp_eq_u32_e32 vcc, v221, v4
	v_or_b32_e32 v7, 19, v217
	s_addc_u32 s1, s45, 0
	s_add_i32 s15, s14, 0x9000
	v_pack_b32_f16 v180, v6, v9
	v_cndmask_b32_e32 v4, 0, v2, vcc
	v_or_b32_e32 v6, 24, v217
	v_cmp_eq_u32_e32 vcc, v221, v7
	s_mov_b32 m0, s15
	s_nop 0
	global_load_lds_dwordx4 v226, s[0:1]
	s_add_u32 s0, s44, 0xb000
	v_pack_b32_f16 v181, v8, v10
	v_cndmask_b32_e32 v7, 0, v2, vcc
	v_cmp_eq_u32_e32 vcc, v221, v6
	v_or_b32_e32 v8, 26, v217
	s_addc_u32 s1, s45, 0
	s_add_i32 s16, s14, 0xb000
	v_cndmask_b32_e32 v6, 0, v2, vcc
	v_or_b32_e32 v9, 25, v217
	v_cmp_eq_u32_e32 vcc, v221, v8
	s_mov_b32 m0, s16
	s_nop 0
	global_load_lds_dwordx4 v226, s[0:1]
	s_add_u32 s0, s44, 0xd000
	v_or_b32_e32 v10, 27, v217
	v_cndmask_b32_e32 v8, 0, v2, vcc
	v_cmp_eq_u32_e32 vcc, v221, v9
	s_addc_u32 s1, s45, 0
	s_add_i32 s16, s14, 0xd000
	v_cndmask_b32_e32 v9, 0, v2, vcc
	v_cmp_eq_u32_e32 vcc, v221, v10
	s_mov_b32 m0, s16
	s_nop 0
	global_load_lds_dwordx4 v226, s[0:1]
	s_add_u32 s0, s44, 0xf000
	s_addc_u32 s1, s45, 0
	v_cndmask_b32_e32 v2, 0, v2, vcc
	s_add_i32 s14, s14, 0xf000
	v_pack_b32_f16 v185, v8, v2
	v_mbcnt_lo_u32_b32 v2, -1, 0
	s_mov_b32 m0, s14
	s_nop 0
	global_load_lds_dwordx4 v226, s[0:1]
	s_add_u32 s0, s44, 0x11000
	v_mbcnt_hi_u32_b32 v2, -1, v2
	s_addc_u32 s1, s45, 0
	s_sub_i32 s12, s15, s12
	v_pack_b32_f16 v183, v4, v7
	v_and_b32_e32 v4, 64, v2
	s_add_i32 s12, s12, 0x8000
	s_mov_b32 m0, s12
	s_nop 0
	global_load_lds_dwordx4 v224, s[0:1]
	v_pack_b32_f16 v182, v3, v5
	v_xor_b32_e32 v3, 32, v2
	v_add_u32_e32 v4, 64, v4
	s_waitcnt vmcnt(0)
	v_cmp_lt_i32_e32 vcc, v3, v4
	s_mov_b32 s13, 0
	v_pack_b32_f16 v184, v6, v9
	v_cndmask_b32_e32 v2, v2, v3, vcc
	v_lshlrev_b32_e32 v225, 2, v2
	v_cmp_gt_u32_e64 s[0:1], 32, v216
	v_lshlrev_b32_e32 v227, 10, v220
	v_lshlrev_b32_e32 v207, 7, v220
	v_lshlrev_b32_e32 v246, 4, v207
	v_lshl_add_u32 v246, v1, 4, v246
	v_lshl_add_u32 v247, v227, 4, v206
	s_mov_b64 s[14:15], -1
	s_mov_b32 s49, 0x2da000
	s_mov_b32 s52, 0x2db000
	s_xor_b64 s[46:47], s[4:5], -1
	s_movk_i32 s53, 0x3844
	s_movk_i32 s54, 0x2bdb
	s_mov_b32 s55, 0xb160
	s_movk_i32 s56, 0x34e2
	s_mov_b32 s57, 0xad10
	s_mov_b32 s58, 0xb1ec
	s_movk_i32 s59, 0x31f0
	s_mov_b32 s60, 0xab4a
	s_brev_b32 s48, 60
	s_mov_b32 s61, 0x800000
	v_mov_b32_e32 v186, 0x43804380
	v_mov_b32_e32 v187, 0
	v_mov_b32_e32 v188, 0xac0d
	s_mov_b32 s62, 0
	s_mov_b32 s33, 0
	s_waitcnt lgkmcnt(0)
	s_barrier
	s_branch .LBB1_8

.LBB1_8:
	s_lshl_b32 s12, s62, 9
	v_lshl_add_u64 v[6:7], s[12:13], 4, v[210:211]
	v_add_co_u32_e32 v34, vcc, s52, v6
	s_mov_b32 s12, s13
	s_nop 0
	v_addc_co_u32_e32 v35, vcc, 0, v7, vcc
	global_load_dwordx4 v[2:5], v[34:35], off offset:-4096
	v_add_co_u32_e32 v36, vcc, s49, v6
	s_xor_b64 s[50:51], s[14:15], -1
	s_nop 0
	v_addc_co_u32_e32 v37, vcc, 0, v7, vcc
	global_load_dwordx4 v[6:9], v[36:37], off offset:1024
	global_load_dwordx4 v[10:13], v[36:37], off offset:2048
	global_load_dwordx4 v[14:17], v[34:35], off
	s_mov_b32 s14, s13
	s_mov_b32 s15, s13
	s_mov_b32 s16, s13
	s_mov_b32 s17, s13
	s_mov_b32 s18, s13
	s_mov_b32 s19, s13
	s_mov_b32 s20, s13
	s_mov_b32 s21, s13
	s_mov_b32 s22, s13
	s_mov_b32 s23, s13
	s_mov_b32 s24, s13
	s_mov_b32 s25, s13
	s_mov_b32 s26, s13
	s_mov_b32 s27, s13
	s_waitcnt vmcnt(3) lgkmcnt(7)
	v_mfma_f32_32x32x16_f16 v[18:33], v[2:5], v[146:149], 0
	global_load_dwordx4 v[2:5], v[36:37], off offset:3072
	s_waitcnt vmcnt(3) lgkmcnt(6)
	v_mfma_f32_32x32x16_f16 v[18:33], v[6:9], v[150:153], v[18:33]
	global_load_dwordx4 v[6:9], v[34:35], off offset:1024
	s_waitcnt vmcnt(3) lgkmcnt(5)
	v_mfma_f32_32x32x16_f16 v[18:33], v[10:13], v[154:157], v[18:33]
	global_load_dwordx4 v[10:13], v[34:35], off offset:2048
	s_nop 0
	global_load_dwordx4 v[34:37], v[34:35], off offset:3072
	s_waitcnt vmcnt(3) lgkmcnt(4)
	v_mfma_f32_32x32x16_f16 v[18:33], v[2:5], v[158:161], v[18:33]
	s_waitcnt lgkmcnt(3)
	v_mfma_f32_32x32x16_f16 v[18:33], v[14:17], v[162:165], v[18:33]
	s_waitcnt vmcnt(2) lgkmcnt(2)
	v_mfma_f32_32x32x16_f16 v[18:33], v[6:9], v[166:169], v[18:33]
	s_waitcnt vmcnt(1) lgkmcnt(1)
	v_mfma_f32_32x32x16_f16 v[18:33], v[10:13], v[170:173], v[18:33]
	v_mov_b64_e32 v[2:3], s[12:13]
	v_mov_b64_e32 v[4:5], s[14:15]
	v_mov_b64_e32 v[6:7], s[16:17]
	v_mov_b64_e32 v[8:9], s[18:19]
	v_mov_b64_e32 v[10:11], s[20:21]
	v_mov_b64_e32 v[12:13], s[22:23]
	v_mov_b64_e32 v[14:15], s[24:25]
	s_waitcnt vmcnt(0) lgkmcnt(0)
	v_mfma_f32_32x32x16_f16 v[18:33], v[34:37], v[174:177], v[18:33]
	v_mov_b64_e32 v[16:17], s[26:27]
	s_mul_i32 s12, s62, 20
	s_lshl_b64 s[14:15], s[12:13], 2
	s_add_u32 s14, s10, s14
	s_addc_u32 s15, s11, s15
	s_load_dwordx16 s[16:31], s[14:15], 0x0
	s_load_dwordx4 s[40:43], s[14:15], 0x40
	s_mul_i32 s12, s62, 0x1b0000
	s_nop 3
	ds_bpermute_b32 v34, v225, v18
	ds_bpermute_b32 v35, v225, v19
	ds_bpermute_b32 v36, v225, v20
	ds_bpermute_b32 v37, v225, v21
	ds_bpermute_b32 v38, v225, v22
	ds_bpermute_b32 v39, v225, v23
	ds_bpermute_b32 v40, v225, v24
	ds_bpermute_b32 v41, v225, v25
	ds_bpermute_b32 v42, v225, v26
	ds_bpermute_b32 v43, v225, v27
	ds_bpermute_b32 v44, v225, v28
	ds_bpermute_b32 v45, v225, v29
	ds_bpermute_b32 v46, v225, v30
	ds_bpermute_b32 v47, v225, v31
	ds_bpermute_b32 v48, v225, v32
	ds_bpermute_b32 v49, v225, v33
	s_waitcnt lgkmcnt(0)
	v_cndmask_b32_e64 v50, v34, v18, s[0:1]
	v_cndmask_b32_e64 v19, v35, v19, s[0:1]
	v_cndmask_b32_e64 v20, v36, v20, s[0:1]
	v_cndmask_b32_e64 v21, v37, v21, s[0:1]
	v_cndmask_b32_e64 v18, v18, v34, s[0:1]
	v_cndmask_b32_e64 v34, v38, v22, s[0:1]
	v_cndmask_b32_e64 v23, v39, v23, s[0:1]
	v_cndmask_b32_e64 v24, v40, v24, s[0:1]
	v_cndmask_b32_e64 v25, v41, v25, s[0:1]
	v_cndmask_b32_e64 v22, v22, v38, s[0:1]
	v_add_f32_e32 v37, s16, v50
	v_add_f32_e32 v19, s17, v19
	v_add_f32_e32 v20, s18, v20
	v_add_f32_e32 v21, s19, v21
	v_add_f32_e32 v34, s21, v34
	v_add_f32_e32 v23, s22, v23
	v_add_f32_e32 v24, s23, v24
	v_add_f32_e32 v25, s24, v25
	v_cndmask_b32_e64 v35, v42, v26, s[0:1]
	v_cndmask_b32_e64 v27, v43, v27, s[0:1]
	v_cndmask_b32_e64 v28, v44, v28, s[0:1]
	v_cndmask_b32_e64 v29, v45, v29, s[0:1]
	v_add_f32_e32 v18, s20, v18
	v_add_f32_e32 v22, s25, v22
	v_max_f32_e32 v38, v37, v19
	v_max_f32_e32 v39, v20, v21
	v_max_f32_e32 v40, v34, v23
	v_max_f32_e32 v41, v24, v25
	v_cndmask_b32_e64 v26, v26, v42, s[0:1]
	v_cndmask_b32_e64 v36, v46, v30, s[0:1]
	v_cndmask_b32_e64 v31, v47, v31, s[0:1]
	v_cndmask_b32_e64 v32, v48, v32, s[0:1]
	v_add_f32_e32 v35, s26, v35
	v_add_f32_e32 v27, s27, v27
	v_add_f32_e32 v28, s28, v28
	v_add_f32_e32 v29, s29, v29
	v_max3_f32 v38, v38, v39, v18
	v_max3_f32 v39, v40, v41, v22
	v_cndmask_b32_e64 v33, v49, v33, s[0:1]
	v_add_f32_e32 v26, s30, v26
	v_add_f32_e32 v36, s31, v36
	v_add_f32_e32 v31, s40, v31
	v_add_f32_e32 v32, s41, v32
	v_max_f32_e32 v42, v35, v27
	v_max_f32_e32 v43, v28, v29
	v_sub_f32_e32 v34, v34, v39
	v_add_f32_e32 v33, s42, v33
	v_cndmask_b32_e64 v30, v30, v46, s[0:1]
	v_max3_f32 v40, v42, v43, v26
	v_sub_f32_e32 v37, v37, v38
	v_sub_f32_e32 v23, v23, v39
	v_mul_f32_e32 v34, 0x3fb8aa3b, v34
	v_add_f32_e32 v30, s43, v30
	v_max_f32_e32 v41, v36, v31
	v_max_f32_e32 v42, v32, v33
	v_sub_f32_e32 v19, v19, v38
	v_sub_f32_e32 v24, v24, v39
	v_sub_f32_e32 v35, v35, v40
	v_mul_f32_e32 v37, 0x3fb8aa3b, v37
	v_mul_f32_e32 v23, 0x3fb8aa3b, v23
	v_exp_f32_e32 v34, v34
	v_max3_f32 v41, v41, v42, v30
	v_sub_f32_e32 v20, v20, v38
	v_sub_f32_e32 v25, v25, v39
	v_sub_f32_e32 v27, v27, v40
	v_mul_f32_e32 v19, 0x3fb8aa3b, v19
	v_mul_f32_e32 v24, 0x3fb8aa3b, v24
	v_mul_f32_e32 v35, 0x3fb8aa3b, v35
	v_exp_f32_e32 v37, v37
	v_exp_f32_e32 v23, v23
	v_sub_f32_e32 v36, v36, v41
	v_sub_f32_e32 v21, v21, v38
	v_sub_f32_e32 v22, v22, v39
	v_sub_f32_e32 v28, v28, v40
	v_mul_f32_e32 v20, 0x3fb8aa3b, v20
	v_mul_f32_e32 v25, 0x3fb8aa3b, v25
	v_mul_f32_e32 v27, 0x3fb8aa3b, v27
	v_exp_f32_e32 v19, v19
	v_exp_f32_e32 v24, v24
	v_exp_f32_e32 v35, v35
	v_mul_f32_e32 v36, 0x3fb8aa3b, v36
	v_sub_f32_e32 v31, v31, v41
	v_sub_f32_e32 v18, v18, v38
	v_sub_f32_e32 v29, v29, v40
	v_mul_f32_e32 v21, 0x3fb8aa3b, v21
	v_mul_f32_e32 v22, 0x3fb8aa3b, v22
	v_mul_f32_e32 v28, 0x3fb8aa3b, v28
	v_exp_f32_e32 v20, v20
	v_exp_f32_e32 v25, v25
	v_exp_f32_e32 v27, v27
	v_exp_f32_e32 v36, v36
	v_mul_f32_e32 v31, 0x3fb8aa3b, v31
	v_sub_f32_e32 v32, v32, v41
	v_sub_f32_e32 v26, v26, v40
	v_mul_f32_e32 v18, 0x3fb8aa3b, v18
	v_mul_f32_e32 v29, 0x3fb8aa3b, v29
	v_exp_f32_e32 v21, v21
	v_exp_f32_e32 v22, v22
	v_exp_f32_e32 v28, v28
	v_add_f32_e32 v39, 0, v34
	v_exp_f32_e32 v31, v31
	v_mul_f32_e32 v32, 0x3fb8aa3b, v32
	v_sub_f32_e32 v33, v33, v41
	v_mul_f32_e32 v26, 0x3fb8aa3b, v26
	v_exp_f32_e32 v18, v18
	v_exp_f32_e32 v29, v29
	v_add_f32_e32 v38, 0, v37
	v_add_f32_e32 v39, v23, v39
	v_exp_f32_e32 v32, v32
	v_mul_f32_e32 v33, 0x3fb8aa3b, v33
	v_sub_f32_e32 v30, v30, v41
	v_exp_f32_e32 v26, v26
	v_add_f32_e32 v40, 0, v35
	v_add_f32_e32 v38, v19, v38
	v_add_f32_e32 v39, v24, v39
	v_exp_f32_e32 v33, v33
	v_mul_f32_e32 v30, 0x3fb8aa3b, v30
	v_add_f32_e32 v40, v27, v40
	v_add_f32_e32 v38, v20, v38
	v_add_f32_e32 v39, v25, v39
	v_add_f32_e32 v42, 0, v36
	v_exp_f32_e32 v30, v30
	v_add_f32_e32 v38, v21, v38
	v_add_f32_e32 v39, v22, v39
	v_add_f32_e32 v40, v28, v40
	v_add_f32_e32 v41, v31, v42
	v_add_f32_e32 v38, v18, v38
	v_rcp_f32_e32 v39, v39
	v_add_f32_e32 v40, v29, v40
	v_add_f32_e32 v41, v32, v41
	v_rcp_f32_e32 v38, v38
	v_add_f32_e32 v40, v26, v40
	v_add_f32_e32 v41, v33, v41
	v_rcp_f32_e32 v40, v40
	v_add_f32_e32 v41, v30, v41
	v_rcp_f32_e32 v41, v41
	v_mul_f32_e32 v34, v34, v39
	v_mul_f32_e32 v23, v23, v39
	v_fmac_f32_e32 v34, v37, v38
	v_fmac_f32_e32 v23, v19, v38
	v_mul_f32_e32 v24, v24, v39
	v_fmac_f32_e32 v34, v35, v40
	v_fmac_f32_e32 v23, v27, v40
	v_mul_f32_e32 v22, v22, v39
	v_mul_f32_e32 v29, v29, v40
	v_fmac_f32_e32 v34, v36, v41
	v_fmac_f32_e32 v23, v31, v41
	v_fmac_f32_e32 v24, v20, v38
	v_fmac_f32_e32 v24, v28, v40
	v_cndmask_b32_e64 v20, v22, v34, s[4:5]
	v_cndmask_b32_e64 v22, v29, v23, s[4:5]
	v_mul_f32_e32 v21, v21, v38
	v_mul_f32_e32 v18, v18, v38
	v_mul_f32_e32 v25, v25, v39
	v_mul_f32_e32 v26, v26, v40
	v_mul_f32_e32 v33, v33, v41
	v_mul_f32_e32 v30, v30, v41
	v_fmac_f32_e32 v24, v32, v41
	v_mul_f32_e32 v20, 0x3e800000, v20
	v_mul_f32_e32 v22, 0x3e800000, v22
	v_mul_f32_e32 v19, 0x3e800000, v25
	ds_write2st64_b32 v222, v20, v22 offset1:8
	v_cndmask_b32_e64 v20, v26, v24, s[4:5]
	v_cndmask_b32_e64 v21, v33, v21, s[4:5]
	v_cndmask_b32_e64 v18, v30, v18, s[4:5]
	v_mul_f32_e32 v20, 0x3e800000, v20
	v_mul_f32_e32 v21, 0x3e800000, v21
	v_mul_f32_e32 v18, 0x3e800000, v18
	v_cndmask_b32_e64 v19, 0, v19, s[4:5]
	ds_write2st64_b32 v222, v20, v21 offset0:16 offset1:24
	ds_write2st64_b32 v222, v18, v19 offset0:32 offset1:40
	s_mul_hi_u32 s14, s62, 0x1b0000
	s_add_u32 s12, s44, s12
	v_mov_b64_e32 v[64:65], v[16:17]
	v_mov_b64_e32 v[48:49], v[16:17]
	v_mov_b64_e32 v[32:33], v[16:17]
	s_addc_u32 s16, s45, s14
	s_mov_b32 s17, 0
	v_mov_b64_e32 v[62:63], v[14:15]
	v_mov_b64_e32 v[60:61], v[12:13]
	v_mov_b64_e32 v[58:59], v[10:11]
	v_mov_b64_e32 v[56:57], v[8:9]
	v_mov_b64_e32 v[54:55], v[6:7]
	v_mov_b64_e32 v[52:53], v[4:5]
	v_mov_b64_e32 v[50:51], v[2:3]
	v_mov_b64_e32 v[46:47], v[14:15]
	v_mov_b64_e32 v[44:45], v[12:13]
	v_mov_b64_e32 v[42:43], v[10:11]
	v_mov_b64_e32 v[40:41], v[8:9]
	v_mov_b64_e32 v[38:39], v[6:7]
	v_mov_b64_e32 v[36:37], v[4:5]
	v_mov_b64_e32 v[34:35], v[2:3]
	v_mov_b64_e32 v[30:31], v[14:15]
	v_mov_b64_e32 v[28:29], v[12:13]
	v_mov_b64_e32 v[26:27], v[10:11]
	v_mov_b64_e32 v[24:25], v[8:9]
	v_mov_b64_e32 v[22:23], v[6:7]
	v_mov_b64_e32 v[20:21], v[4:5]
	v_mov_b64_e32 v[18:19], v[2:3]
	s_mov_b32 s18, 0
	s_mul_i32 s25, s33, 0x9000
	s_add_i32 s26, s33, -1
	s_cmp_eq_u32 s33, 0
	s_cselect_b32 s26, 2, s26
	s_mul_i32 s26, s26, 0x9000
	s_cmp_lg_u32 s4, 0
	s_cselect_b32 s27, 0x7fffffff, 40
	s_branch .LBB1_10

.Lnf_9b:
	s_mov_b32 s26, s25
	s_add_i32 s25, s25, 0x9000
	s_cmp_lg_u32 s26, 0x12000
	s_cselect_b32 s25, s25, 0
	s_add_i32 s18, s18, 1
	s_add_u32 s12, s12, 0x9000
	s_addc_u32 s16, s16, 0
	s_cmp_eq_u32 s18, 48
	s_waitcnt vmcnt(5) lgkmcnt(0)
	s_barrier
	s_cbranch_scc1 .LBB1_19
.LBB1_10:
	s_cmp_ge_u32 s18, s27
	s_cbranch_scc1 .Lnf_inact
	s_add_i32 s22, s25, 0x8000
	s_and_b32 s19, s18, 7
	s_cmp_lg_u32 s19, 0
	v_add_u32_e32 v189, s22, v246
	s_cbranch_scc1 .LBB1_15
	ds_read_b128 v[66:69], v189 offset:33280
	ds_read_b128 v[70:73], v189 offset:33312
	ds_read_b128 v[74:77], v189 offset:33344
	ds_read_b128 v[78:81], v189 offset:33376
	ds_read_b128 v[82:85], v189 offset:33408
	ds_read_b128 v[86:89], v189 offset:33440
	ds_read_b128 v[90:93], v189 offset:33472
	ds_read_b128 v[94:97], v189 offset:33504
	ds_read_b128 v[98:101], v189 offset:33536
	ds_read_b128 v[102:105], v189 offset:33568
	ds_read_b128 v[106:109], v189 offset:33600
	ds_read_b128 v[110:113], v189 offset:33632
	ds_read_b128 v[114:117], v189 offset:33664
	ds_read_b128 v[118:121], v189 offset:33696
	ds_read_b128 v[122:125], v189 offset:33728
	ds_read_b128 v[126:129], v189 offset:33760
	s_waitcnt lgkmcnt(12)
	v_mfma_f32_32x32x16_f16 v[66:81], v[178:181], v[146:149], v[66:81]
	s_waitcnt lgkmcnt(8)
	v_mfma_f32_32x32x16_f16 v[82:97], v[178:181], v[154:157], v[82:97]
	s_waitcnt lgkmcnt(4)
	v_mfma_f32_32x32x16_f16 v[98:113], v[178:181], v[162:165], v[98:113]
	s_waitcnt lgkmcnt(0)
	v_mfma_f32_32x32x16_f16 v[114:129], v[178:181], v[170:173], v[114:129]
	v_mfma_f32_32x32x16_f16 v[66:81], v[182:185], v[150:153], v[66:81]
	v_mfma_f32_32x32x16_f16 v[82:97], v[182:185], v[158:161], v[82:97]
	v_mfma_f32_32x32x16_f16 v[98:113], v[182:185], v[166:169], v[98:113]
	v_mfma_f32_32x32x16_f16 v[114:129], v[182:185], v[174:177], v[114:129]
.LBB1_15:
	v_add_u32_e32 v240, s25, v247
	ds_read_b128 v[130:133], v189 offset:32768
	ds_read_b128 v[134:137], v189 offset:32800
	ds_read_b128 v[138:141], v189 offset:32832
	ds_read_b128 v[142:145], v189 offset:32864
	ds_read_b128 v[190:193], v240 offset:32768
	ds_read_b128 v[194:197], v240 offset:33792
	ds_read_b128 v[198:201], v240 offset:34816
	ds_read_b128 v[202:205], v240 offset:35840
	ds_read_b128 v[212:215], v240 offset:36864
	ds_read_b128 v[228:231], v240 offset:37888
	ds_read_b128 v[232:235], v240 offset:38912
	ds_read_b128 v[236:239], v240 offset:39936
	s_waitcnt lgkmcnt(7)
	v_mfma_f32_32x32x16_f16 v[130:145], v[190:193], v[146:149], v[130:145]
	s_waitcnt lgkmcnt(6)
	v_mfma_f32_32x32x16_f16 v[130:145], v[194:197], v[150:153], v[130:145]
	s_waitcnt lgkmcnt(5)
	v_mfma_f32_32x32x16_f16 v[130:145], v[198:201], v[154:157], v[130:145]
	s_waitcnt lgkmcnt(4)
	v_mfma_f32_32x32x16_f16 v[130:145], v[202:205], v[158:161], v[130:145]
	v_readfirstlane_b32 s21, v0
	s_lshl_b32 s22, s21, 4
	s_and_b32 s21, s22, 0xfffffc00
	s_add_i32 s20, s21, s26
	s_cmp_lg_u32 s3, -1
	s_cselect_b32 s21, s3, 0
	s_add_i32 s23, s20, s21
	s_add_u32 s20, s12, 0x12000
	s_addc_u32 s21, s16, 0
	s_mov_b32 m0, s23
	s_nop 0
	global_load_lds_dwordx4 v226, s[20:21]
	s_waitcnt lgkmcnt(3)
	v_mfma_f32_32x32x16_f16 v[130:145], v[212:215], v[162:165], v[130:145]
	s_add_u32 s20, s12, 0x14000
	s_addc_u32 s21, s16, 0
	s_add_i32 s24, s23, 0x2000
	s_mov_b32 m0, s24
	s_nop 0
	global_load_lds_dwordx4 v226, s[20:21]
	s_waitcnt lgkmcnt(2)
	v_mfma_f32_32x32x16_f16 v[130:145], v[228:231], v[166:169], v[130:145]
	s_add_u32 s20, s12, 0x16000
	s_addc_u32 s21, s16, 0
	s_add_i32 s24, s23, 0x4000
	s_mov_b32 m0, s24
	s_nop 0
	global_load_lds_dwordx4 v226, s[20:21]
	s_waitcnt lgkmcnt(1)
	v_mfma_f32_32x32x16_f16 v[130:145], v[232:235], v[170:173], v[130:145]
	s_add_u32 s20, s12, 0x18000
	s_addc_u32 s21, s16, 0
	s_add_i32 s24, s23, 0x6000
	s_mov_b32 m0, s24
	s_nop 0
	global_load_lds_dwordx4 v226, s[20:21]
	s_waitcnt lgkmcnt(0)
	v_mfma_f32_32x32x16_f16 v[130:145], v[236:239], v[174:177], v[130:145]
	s_add_u32 s20, s12, 0x1a000
	s_addc_u32 s21, s16, 0
	s_and_b32 s22, s22, 0xfffff000
	s_sub_i32 s22, s23, s22
	s_add_i32 s22, s22, 0x8000
	s_mov_b32 m0, s22
	s_nop 0
	global_load_lds_dwordx4 v224, s[20:21]
	ds_read_b128 v[190:193], v240 offset:40960
	ds_read_b128 v[194:197], v240 offset:41984
	ds_read_b128 v[198:201], v240 offset:43008
	ds_read_b128 v[202:205], v240 offset:44032
	ds_read_b128 v[212:215], v240 offset:45056
	ds_read_b128 v[228:231], v240 offset:46080
	ds_read_b128 v[232:235], v240 offset:47104
	ds_read_b128 v[236:239], v240 offset:48128
	v_cvt_pk_f16_f32 v130, v130, v131
	v_cvt_pk_f16_f32 v131, v132, v133
	v_cvt_pk_f16_f32 v132, v134, v135
	v_cvt_pk_f16_f32 v133, v136, v137
	v_and_b32_e32 v134, 0x7fff7fff, v130
	v_and_b32_e32 v135, 0x7fff7fff, v131
	v_and_b32_e32 v136, 0x7fff7fff, v132
	v_and_b32_e32 v137, 0x7fff7fff, v133
	v_pk_min_f16 v134, v134, v186
	v_pk_min_f16 v135, v135, v186
	v_pk_min_f16 v136, v136, v186
	v_pk_min_f16 v137, v137, v186
	v_pk_max_f16 v130, v130, v187
	v_pk_max_f16 v131, v131, v187
	s_nop 0
	v_pk_fma_f16 v134, v134, s53, -1.0 op_sel_hi:[1,0,0]
	v_pk_fma_f16 v135, v135, s53, -1.0 op_sel_hi:[1,0,0]
	v_pk_fma_f16 v136, v136, s53, -1.0 op_sel_hi:[1,0,0]
	v_pk_fma_f16 v137, v137, s53, -1.0 op_sel_hi:[1,0,0]
	v_pk_fma_f16 v240, v134, s54, v188 op_sel_hi:[1,0,0]
	v_pk_fma_f16 v241, v135, s54, v188 op_sel_hi:[1,0,0]
	v_pk_fma_f16 v242, v136, s54, v188 op_sel_hi:[1,0,0]
	v_pk_fma_f16 v243, v137, s54, v188 op_sel_hi:[1,0,0]
	v_pk_fma_f16 v240, v134, v240, s55 op_sel_hi:[1,1,0]
	v_pk_fma_f16 v241, v135, v241, s55 op_sel_hi:[1,1,0]
	v_pk_fma_f16 v242, v136, v242, s55 op_sel_hi:[1,1,0]
	v_pk_fma_f16 v243, v137, v243, s55 op_sel_hi:[1,1,0]
	v_pk_fma_f16 v240, v134, v240, s56 op_sel_hi:[1,1,0]
	v_pk_fma_f16 v241, v135, v241, s56 op_sel_hi:[1,1,0]
	v_pk_fma_f16 v242, v136, v242, s56 op_sel_hi:[1,1,0]
	v_pk_fma_f16 v243, v137, v243, s56 op_sel_hi:[1,1,0]
	v_pk_fma_f16 v240, v134, v240, s57 op_sel_hi:[1,1,0]
	v_pk_fma_f16 v241, v135, v241, s57 op_sel_hi:[1,1,0]
	v_pk_fma_f16 v242, v136, v242, s57 op_sel_hi:[1,1,0]
	v_pk_fma_f16 v243, v137, v243, s57 op_sel_hi:[1,1,0]
	v_pk_fma_f16 v240, v134, v240, s58 op_sel_hi:[1,1,0]
	v_pk_fma_f16 v241, v135, v241, s58 op_sel_hi:[1,1,0]
	v_pk_fma_f16 v242, v136, v242, s58 op_sel_hi:[1,1,0]
	v_pk_fma_f16 v243, v137, v243, s58 op_sel_hi:[1,1,0]
	v_pk_fma_f16 v240, v134, v240, s59 op_sel_hi:[1,1,0]
	v_pk_fma_f16 v241, v135, v241, s59 op_sel_hi:[1,1,0]
	v_pk_fma_f16 v242, v136, v242, s59 op_sel_hi:[1,1,0]
	v_pk_fma_f16 v243, v137, v243, s59 op_sel_hi:[1,1,0]
	v_pk_max_f16 v132, v132, v187
	v_pk_max_f16 v133, v133, v187
	v_pk_fma_f16 v134, v134, v240, s60 op_sel_hi:[1,1,0]
	v_pk_fma_f16 v135, v135, v241, s60 op_sel_hi:[1,1,0]
	v_pk_fma_f16 v136, v136, v242, s60 op_sel_hi:[1,1,0]
	v_pk_fma_f16 v137, v137, v243, s60 op_sel_hi:[1,1,0]
	v_pk_add_f16 v130, v130, v134
	v_pk_add_f16 v131, v131, v135
	v_pk_add_f16 v132, v132, v136
	v_pk_add_f16 v133, v133, v137
	v_cvt_pk_f16_f32 v134, v138, v139
	v_cvt_pk_f16_f32 v135, v140, v141
	v_cvt_pk_f16_f32 v136, v142, v143
	v_cvt_pk_f16_f32 v137, v144, v145
	v_and_b32_e32 v138, 0x7fff7fff, v134
	v_and_b32_e32 v139, 0x7fff7fff, v135
	v_and_b32_e32 v140, 0x7fff7fff, v136
	v_and_b32_e32 v141, 0x7fff7fff, v137
	v_pk_min_f16 v138, v138, v186
	v_pk_min_f16 v139, v139, v186
	v_pk_min_f16 v140, v140, v186
	v_pk_min_f16 v141, v141, v186
	s_waitcnt lgkmcnt(7)
	v_mfma_f32_32x32x16_f16 v[66:81], v[190:193], v[130:133], v[66:81]
	v_pk_fma_f16 v138, v138, s53, -1.0 op_sel_hi:[1,0,0]
	v_pk_fma_f16 v139, v139, s53, -1.0 op_sel_hi:[1,0,0]
	v_pk_fma_f16 v140, v140, s53, -1.0 op_sel_hi:[1,0,0]
	v_pk_fma_f16 v141, v141, s53, -1.0 op_sel_hi:[1,0,0]
	v_pk_fma_f16 v142, v138, s54, v188 op_sel_hi:[1,0,0]
	v_pk_fma_f16 v143, v139, s54, v188 op_sel_hi:[1,0,0]
	v_pk_fma_f16 v144, v140, s54, v188 op_sel_hi:[1,0,0]
	v_pk_fma_f16 v145, v141, s54, v188 op_sel_hi:[1,0,0]
	s_waitcnt lgkmcnt(5)
	v_mfma_f32_32x32x16_f16 v[82:97], v[198:201], v[130:133], v[82:97]
	v_pk_fma_f16 v142, v138, v142, s55 op_sel_hi:[1,1,0]
	v_pk_fma_f16 v143, v139, v143, s55 op_sel_hi:[1,1,0]
	v_pk_fma_f16 v144, v140, v144, s55 op_sel_hi:[1,1,0]
	v_pk_fma_f16 v145, v141, v145, s55 op_sel_hi:[1,1,0]
	v_pk_fma_f16 v142, v138, v142, s56 op_sel_hi:[1,1,0]
	v_pk_fma_f16 v143, v139, v143, s56 op_sel_hi:[1,1,0]
	v_pk_fma_f16 v144, v140, v144, s56 op_sel_hi:[1,1,0]
	s_waitcnt lgkmcnt(3)
	v_mfma_f32_32x32x16_f16 v[98:113], v[212:215], v[130:133], v[98:113]
	v_pk_fma_f16 v145, v141, v145, s56 op_sel_hi:[1,1,0]
	v_pk_fma_f16 v142, v138, v142, s57 op_sel_hi:[1,1,0]
	v_pk_fma_f16 v143, v139, v143, s57 op_sel_hi:[1,1,0]
	v_pk_fma_f16 v144, v140, v144, s57 op_sel_hi:[1,1,0]
	v_pk_fma_f16 v145, v141, v145, s57 op_sel_hi:[1,1,0]
	v_pk_fma_f16 v142, v138, v142, s58 op_sel_hi:[1,1,0]
	v_pk_fma_f16 v143, v139, v143, s58 op_sel_hi:[1,1,0]
	s_waitcnt lgkmcnt(1)
	v_mfma_f32_32x32x16_f16 v[114:129], v[232:235], v[130:133], v[114:129]
	v_pk_fma_f16 v144, v140, v144, s58 op_sel_hi:[1,1,0]
	v_pk_fma_f16 v145, v141, v145, s58 op_sel_hi:[1,1,0]
	v_pk_fma_f16 v142, v138, v142, s59 op_sel_hi:[1,1,0]
	v_pk_fma_f16 v143, v139, v143, s59 op_sel_hi:[1,1,0]
	v_pk_fma_f16 v144, v140, v144, s59 op_sel_hi:[1,1,0]
	v_pk_fma_f16 v145, v141, v145, s59 op_sel_hi:[1,1,0]
	v_pk_max_f16 v134, v134, v187
	v_pk_max_f16 v135, v135, v187
	v_pk_max_f16 v136, v136, v187
	v_pk_max_f16 v137, v137, v187
	v_pk_fma_f16 v138, v138, v142, s60 op_sel_hi:[1,1,0]
	v_pk_fma_f16 v139, v139, v143, s60 op_sel_hi:[1,1,0]
	v_pk_fma_f16 v140, v140, v144, s60 op_sel_hi:[1,1,0]
	v_pk_fma_f16 v141, v141, v145, s60 op_sel_hi:[1,1,0]
	v_pk_add_f16 v134, v134, v138
	v_pk_add_f16 v135, v135, v139
	v_pk_add_f16 v136, v136, v140
	v_pk_add_f16 v137, v137, v141
	s_cmp_lg_u32 s19, 7
	s_nop 0
	v_mfma_f32_32x32x16_f16 v[66:81], v[194:197], v[134:137], v[66:81]
	v_mfma_f32_32x32x16_f16 v[82:97], v[202:205], v[134:137], v[82:97]
	v_mfma_f32_32x32x16_f16 v[98:113], v[228:231], v[134:137], v[98:113]
	s_waitcnt lgkmcnt(0)
	v_mfma_f32_32x32x16_f16 v[114:129], v[236:239], v[134:137], v[114:129]
	s_cbranch_scc1 .LBB1_17
	ds_read_b128 v[132:135], v189 offset:33312
	ds_read_b128 v[136:139], v189 offset:33344
	ds_read_b128 v[140:143], v189 offset:33824
	ds_read_b128 v[190:193], v189 offset:33856
	ds_read_b128 v[194:197], v189 offset:33792
	ds_read_b128 v[198:201], v189 offset:33376
	ds_read_b128 v[202:205], v189 offset:33888
	s_lshl_b32 s19, s18, 6
	s_and_b32 s19, s19, 0xe00
	v_lshl_add_u32 v130, s19, 2, v222
	ds_read_b128 v[212:215], v189 offset:33280
	ds_read_b32 v130, v130
	v_pk_add_f32 v[144:145], v[66:67], v[68:69]
	v_pk_mul_f32 v[228:229], v[66:67], v[66:67]
	v_pk_add_f32 v[230:231], v[82:83], v[84:85]
	v_pk_mul_f32 v[232:233], v[82:83], v[82:83]
	v_pk_add_f32 v[234:235], v[98:99], v[100:101]
	v_pk_mul_f32 v[236:237], v[98:99], v[98:99]
	v_pk_add_f32 v[238:239], v[114:115], v[116:117]
	v_pk_mul_f32 v[240:241], v[114:115], v[114:115]
	v_pk_fma_f32 v[228:229], v[68:69], v[68:69], v[228:229]
	v_pk_fma_f32 v[232:233], v[84:85], v[84:85], v[232:233]
	v_pk_fma_f32 v[236:237], v[100:101], v[100:101], v[236:237]
	v_pk_fma_f32 v[240:241], v[116:117], v[116:117], v[240:241]
	v_pk_add_f32 v[144:145], v[70:71], v[144:145]
	v_pk_add_f32 v[230:231], v[86:87], v[230:231]
	v_pk_add_f32 v[234:235], v[102:103], v[234:235]
	v_pk_add_f32 v[238:239], v[118:119], v[238:239]
	v_pk_fma_f32 v[228:229], v[70:71], v[70:71], v[228:229]
	v_pk_fma_f32 v[232:233], v[86:87], v[86:87], v[232:233]
	v_pk_fma_f32 v[236:237], v[102:103], v[102:103], v[236:237]
	v_pk_fma_f32 v[240:241], v[118:119], v[118:119], v[240:241]
	v_pk_add_f32 v[144:145], v[72:73], v[144:145]
	v_pk_add_f32 v[230:231], v[88:89], v[230:231]
	v_pk_add_f32 v[234:235], v[104:105], v[234:235]
	v_pk_add_f32 v[238:239], v[120:121], v[238:239]
	v_pk_fma_f32 v[228:229], v[72:73], v[72:73], v[228:229]
	v_pk_fma_f32 v[232:233], v[88:89], v[88:89], v[232:233]
	v_pk_fma_f32 v[236:237], v[104:105], v[104:105], v[236:237]
	v_pk_fma_f32 v[240:241], v[120:121], v[120:121], v[240:241]
	v_pk_add_f32 v[144:145], v[74:75], v[144:145]
	v_pk_add_f32 v[230:231], v[90:91], v[230:231]
	v_pk_add_f32 v[234:235], v[106:107], v[234:235]
	v_pk_add_f32 v[238:239], v[122:123], v[238:239]
	v_pk_fma_f32 v[228:229], v[74:75], v[74:75], v[228:229]
	v_pk_fma_f32 v[232:233], v[90:91], v[90:91], v[232:233]
	v_pk_fma_f32 v[236:237], v[106:107], v[106:107], v[236:237]
	v_pk_fma_f32 v[240:241], v[122:123], v[122:123], v[240:241]
	v_pk_add_f32 v[144:145], v[76:77], v[144:145]
	v_pk_add_f32 v[230:231], v[92:93], v[230:231]
	v_pk_add_f32 v[234:235], v[108:109], v[234:235]
	v_pk_add_f32 v[238:239], v[124:125], v[238:239]
	v_pk_fma_f32 v[228:229], v[76:77], v[76:77], v[228:229]
	v_pk_fma_f32 v[232:233], v[92:93], v[92:93], v[232:233]
	v_pk_fma_f32 v[236:237], v[108:109], v[108:109], v[236:237]
	v_pk_fma_f32 v[240:241], v[124:125], v[124:125], v[240:241]
	v_pk_add_f32 v[144:145], v[78:79], v[144:145]
	v_pk_add_f32 v[230:231], v[94:95], v[230:231]
	v_pk_add_f32 v[234:235], v[110:111], v[234:235]
	v_pk_add_f32 v[238:239], v[126:127], v[238:239]
	v_pk_fma_f32 v[228:229], v[78:79], v[78:79], v[228:229]
	v_pk_fma_f32 v[232:233], v[94:95], v[94:95], v[232:233]
	v_pk_fma_f32 v[236:237], v[110:111], v[110:111], v[236:237]
	v_pk_fma_f32 v[240:241], v[126:127], v[126:127], v[240:241]
	v_pk_add_f32 v[144:145], v[80:81], v[144:145]
	v_pk_add_f32 v[230:231], v[96:97], v[230:231]
	v_pk_add_f32 v[234:235], v[112:113], v[234:235]
	v_pk_add_f32 v[238:239], v[128:129], v[238:239]
	v_pk_fma_f32 v[228:229], v[80:81], v[80:81], v[228:229]
	v_pk_fma_f32 v[232:233], v[96:97], v[96:97], v[232:233]
	v_pk_fma_f32 v[236:237], v[112:113], v[112:113], v[236:237]
	v_pk_fma_f32 v[240:241], v[128:129], v[128:129], v[240:241]
	v_pk_add_f32 v[144:145], v[144:145], v[230:231]
	v_pk_add_f32 v[230:231], v[234:235], v[238:239]
	v_pk_add_f32 v[228:229], v[228:229], v[232:233]
	v_pk_add_f32 v[144:145], v[144:145], v[230:231]
	v_pk_add_f32 v[230:231], v[236:237], v[240:241]
	s_nop 0
	v_pk_add_f32 v[228:229], v[228:229], v[230:231]
	v_mov_b32_e32 v231, v144
	v_mov_b32_e32 v230, v228
	v_mov_b32_e32 v144, v229
	v_pk_add_f32 v[144:145], v[230:231], v[144:145]
	ds_bpermute_b32 v229, v225, v145
	ds_bpermute_b32 v228, v225, v144
	s_waitcnt lgkmcnt(0)
	v_pk_add_f32 v[144:145], v[144:145], v[228:229]
	s_nop 0
	v_pk_mul_f32 v[144:145], v[144:145], s[48:49] op_sel_hi:[1,0]
	s_nop 0
	v_fma_f32 v131, -v145, v145, v144
	v_add_f32_e32 v131, 0x3727c5ac, v131
	v_mul_f32_e32 v144, 0x4b800000, v131
	v_cmp_gt_f32_e32 vcc, s61, v131
	s_nop 1
	v_cndmask_b32_e32 v131, v131, v144, vcc
	v_rsq_f32_e32 v131, v131
	s_nop 0
	v_mul_f32_e32 v144, 0x45800000, v131
	v_cndmask_b32_e32 v144, v131, v144, vcc
	v_mul_f32_e64 v228, v144, -v145
	v_pk_fma_f32 v[230:231], v[80:81], v[144:145], v[228:229] op_sel_hi:[1,0,0]
	v_pk_fma_f32 v[232:233], v[78:79], v[144:145], v[228:229] op_sel_hi:[1,0,0]
	v_pk_fma_f32 v[234:235], v[76:77], v[144:145], v[228:229] op_sel_hi:[1,0,0]
	v_pk_fma_f32 v[236:237], v[74:75], v[144:145], v[228:229] op_sel_hi:[1,0,0]
	v_pk_fma_f32 v[238:239], v[72:73], v[144:145], v[228:229] op_sel_hi:[1,0,0]
	v_pk_fma_f32 v[240:241], v[70:71], v[144:145], v[228:229] op_sel_hi:[1,0,0]
	v_pk_fma_f32 v[242:243], v[68:69], v[144:145], v[228:229] op_sel_hi:[1,0,0]
	v_pk_fma_f32 v[244:245], v[66:67], v[144:145], v[228:229] op_sel_hi:[1,0,0]
	v_pk_fma_f32 v[196:197], v[242:243], v[214:215], v[196:197]
	v_pk_fma_f32 v[194:195], v[244:245], v[212:213], v[194:195]
	v_pk_fma_f32 v[132:133], v[240:241], v[132:133], v[140:141]
	v_pk_fma_f32 v[134:135], v[238:239], v[134:135], v[142:143]
	v_pk_fma_f32 v[136:137], v[236:237], v[136:137], v[190:191]
	v_pk_fma_f32 v[138:139], v[234:235], v[138:139], v[192:193]
	v_pk_fma_f32 v[140:141], v[232:233], v[198:199], v[202:203]
	v_pk_fma_f32 v[142:143], v[230:231], v[200:201], v[204:205]
	v_pk_fma_f32 v[14:15], v[130:131], v[140:141], v[14:15] op_sel_hi:[0,1,1]
	v_pk_fma_f32 v[16:17], v[130:131], v[142:143], v[16:17] op_sel_hi:[0,1,1]
	v_pk_fma_f32 v[12:13], v[130:131], v[138:139], v[12:13] op_sel_hi:[0,1,1]
	v_pk_fma_f32 v[10:11], v[130:131], v[136:137], v[10:11] op_sel_hi:[0,1,1]
	v_pk_fma_f32 v[8:9], v[130:131], v[134:135], v[8:9] op_sel_hi:[0,1,1]
	v_pk_fma_f32 v[6:7], v[130:131], v[132:133], v[6:7] op_sel_hi:[0,1,1]
	v_pk_fma_f32 v[4:5], v[130:131], v[196:197], v[4:5] op_sel_hi:[0,1,1]
	v_pk_fma_f32 v[2:3], v[130:131], v[194:195], v[2:3] op_sel_hi:[0,1,1]
	ds_read_b128 v[132:135], v189 offset:33408
	ds_read_b128 v[136:139], v189 offset:33440
	ds_read_b128 v[140:143], v189 offset:33920
	ds_read_b128 v[190:193], v189 offset:33952
	ds_read_b128 v[194:197], v189 offset:33472
	ds_read_b128 v[198:201], v189 offset:33504
	ds_read_b128 v[202:205], v189 offset:33984
	ds_read_b128 v[212:215], v189 offset:34016
	v_pk_fma_f32 v[230:231], v[96:97], v[144:145], v[228:229] op_sel_hi:[1,0,0]
	v_pk_fma_f32 v[232:233], v[94:95], v[144:145], v[228:229] op_sel_hi:[1,0,0]
	v_pk_fma_f32 v[234:235], v[92:93], v[144:145], v[228:229] op_sel_hi:[1,0,0]
	v_pk_fma_f32 v[236:237], v[90:91], v[144:145], v[228:229] op_sel_hi:[1,0,0]
	v_pk_fma_f32 v[238:239], v[88:89], v[144:145], v[228:229] op_sel_hi:[1,0,0]
	v_pk_fma_f32 v[240:241], v[86:87], v[144:145], v[228:229] op_sel_hi:[1,0,0]
	v_pk_fma_f32 v[242:243], v[84:85], v[144:145], v[228:229] op_sel_hi:[1,0,0]
	v_pk_fma_f32 v[244:245], v[82:83], v[144:145], v[228:229] op_sel_hi:[1,0,0]
	s_waitcnt lgkmcnt(5)
	v_pk_fma_f32 v[134:135], v[242:243], v[134:135], v[142:143]
	v_pk_fma_f32 v[132:133], v[244:245], v[132:133], v[140:141]
	s_waitcnt lgkmcnt(4)
	v_pk_fma_f32 v[136:137], v[240:241], v[136:137], v[190:191]
	v_pk_fma_f32 v[138:139], v[238:239], v[138:139], v[192:193]
	s_waitcnt lgkmcnt(1)
	v_pk_fma_f32 v[140:141], v[236:237], v[194:195], v[202:203]
	v_pk_fma_f32 v[142:143], v[234:235], v[196:197], v[204:205]
	s_waitcnt lgkmcnt(0)
	v_pk_fma_f32 v[190:191], v[232:233], v[198:199], v[212:213]
	v_pk_fma_f32 v[192:193], v[230:231], v[200:201], v[214:215]
	v_pk_fma_f32 v[62:63], v[130:131], v[190:191], v[62:63] op_sel_hi:[0,1,1]
	v_pk_fma_f32 v[64:65], v[130:131], v[192:193], v[64:65] op_sel_hi:[0,1,1]
	v_pk_fma_f32 v[60:61], v[130:131], v[142:143], v[60:61] op_sel_hi:[0,1,1]
	v_pk_fma_f32 v[58:59], v[130:131], v[140:141], v[58:59] op_sel_hi:[0,1,1]
	v_pk_fma_f32 v[56:57], v[130:131], v[138:139], v[56:57] op_sel_hi:[0,1,1]
	v_pk_fma_f32 v[54:55], v[130:131], v[136:137], v[54:55] op_sel_hi:[0,1,1]
	v_pk_fma_f32 v[52:53], v[130:131], v[134:135], v[52:53] op_sel_hi:[0,1,1]
	v_pk_fma_f32 v[50:51], v[130:131], v[132:133], v[50:51] op_sel_hi:[0,1,1]
	ds_read_b128 v[132:135], v189 offset:33536
	ds_read_b128 v[136:139], v189 offset:33568
	ds_read_b128 v[140:143], v189 offset:34048
	ds_read_b128 v[190:193], v189 offset:34080
	ds_read_b128 v[194:197], v189 offset:33600
	ds_read_b128 v[198:201], v189 offset:33632
	ds_read_b128 v[202:205], v189 offset:34112
	ds_read_b128 v[212:215], v189 offset:34144
	v_pk_fma_f32 v[230:231], v[112:113], v[144:145], v[228:229] op_sel_hi:[1,0,0]
	v_pk_fma_f32 v[232:233], v[110:111], v[144:145], v[228:229] op_sel_hi:[1,0,0]
	v_pk_fma_f32 v[234:235], v[108:109], v[144:145], v[228:229] op_sel_hi:[1,0,0]
	v_pk_fma_f32 v[236:237], v[106:107], v[144:145], v[228:229] op_sel_hi:[1,0,0]
	v_pk_fma_f32 v[238:239], v[104:105], v[144:145], v[228:229] op_sel_hi:[1,0,0]
	v_pk_fma_f32 v[240:241], v[102:103], v[144:145], v[228:229] op_sel_hi:[1,0,0]
	v_pk_fma_f32 v[242:243], v[100:101], v[144:145], v[228:229] op_sel_hi:[1,0,0]
	v_pk_fma_f32 v[244:245], v[98:99], v[144:145], v[228:229] op_sel_hi:[1,0,0]
	s_waitcnt lgkmcnt(5)
	v_pk_fma_f32 v[134:135], v[242:243], v[134:135], v[142:143]
	v_pk_fma_f32 v[132:133], v[244:245], v[132:133], v[140:141]
	s_waitcnt lgkmcnt(4)
	v_pk_fma_f32 v[136:137], v[240:241], v[136:137], v[190:191]
	v_pk_fma_f32 v[138:139], v[238:239], v[138:139], v[192:193]
	s_waitcnt lgkmcnt(1)
	v_pk_fma_f32 v[140:141], v[236:237], v[194:195], v[202:203]
	v_pk_fma_f32 v[142:143], v[234:235], v[196:197], v[204:205]
	s_waitcnt lgkmcnt(0)
	v_pk_fma_f32 v[190:191], v[232:233], v[198:199], v[212:213]
	v_pk_fma_f32 v[192:193], v[230:231], v[200:201], v[214:215]
	v_pk_fma_f32 v[46:47], v[130:131], v[190:191], v[46:47] op_sel_hi:[0,1,1]
	v_pk_fma_f32 v[48:49], v[130:131], v[192:193], v[48:49] op_sel_hi:[0,1,1]
	v_pk_fma_f32 v[44:45], v[130:131], v[142:143], v[44:45] op_sel_hi:[0,1,1]
	v_pk_fma_f32 v[42:43], v[130:131], v[140:141], v[42:43] op_sel_hi:[0,1,1]
	v_pk_fma_f32 v[40:41], v[130:131], v[138:139], v[40:41] op_sel_hi:[0,1,1]
	v_pk_fma_f32 v[38:39], v[130:131], v[136:137], v[38:39] op_sel_hi:[0,1,1]
	v_pk_fma_f32 v[36:37], v[130:131], v[134:135], v[36:37] op_sel_hi:[0,1,1]
	v_pk_fma_f32 v[34:35], v[130:131], v[132:133], v[34:35] op_sel_hi:[0,1,1]
	ds_read_b128 v[132:135], v189 offset:33664
	ds_read_b128 v[136:139], v189 offset:33696
	ds_read_b128 v[140:143], v189 offset:34176
	ds_read_b128 v[190:193], v189 offset:34208
	ds_read_b128 v[194:197], v189 offset:33728
	ds_read_b128 v[198:201], v189 offset:33760
	ds_read_b128 v[202:205], v189 offset:34240
	ds_read_b128 v[212:215], v189 offset:34272
	v_pk_fma_f32 v[230:231], v[128:129], v[144:145], v[228:229] op_sel_hi:[1,0,0]
	v_pk_fma_f32 v[232:233], v[126:127], v[144:145], v[228:229] op_sel_hi:[1,0,0]
	v_pk_fma_f32 v[234:235], v[124:125], v[144:145], v[228:229] op_sel_hi:[1,0,0]
	v_pk_fma_f32 v[236:237], v[122:123], v[144:145], v[228:229] op_sel_hi:[1,0,0]
	v_pk_fma_f32 v[238:239], v[120:121], v[144:145], v[228:229] op_sel_hi:[1,0,0]
	v_pk_fma_f32 v[240:241], v[118:119], v[144:145], v[228:229] op_sel_hi:[1,0,0]
	v_pk_fma_f32 v[242:243], v[116:117], v[144:145], v[228:229] op_sel_hi:[1,0,0]
	v_pk_fma_f32 v[144:145], v[114:115], v[144:145], v[228:229] op_sel_hi:[1,0,0]
	s_waitcnt lgkmcnt(5)
	v_pk_fma_f32 v[134:135], v[242:243], v[134:135], v[142:143]
	v_pk_fma_f32 v[132:133], v[144:145], v[132:133], v[140:141]
	s_waitcnt lgkmcnt(4)
	v_pk_fma_f32 v[136:137], v[240:241], v[136:137], v[190:191]
	v_pk_fma_f32 v[138:139], v[238:239], v[138:139], v[192:193]
	s_waitcnt lgkmcnt(1)
	v_pk_fma_f32 v[140:141], v[236:237], v[194:195], v[202:203]
	v_pk_fma_f32 v[142:143], v[234:235], v[196:197], v[204:205]
	s_waitcnt lgkmcnt(0)
	v_pk_fma_f32 v[144:145], v[232:233], v[198:199], v[212:213]
	v_pk_fma_f32 v[190:191], v[230:231], v[200:201], v[214:215]
	v_pk_fma_f32 v[30:31], v[130:131], v[144:145], v[30:31] op_sel_hi:[0,1,1]
	v_pk_fma_f32 v[32:33], v[130:131], v[190:191], v[32:33] op_sel_hi:[0,1,1]
	v_pk_fma_f32 v[28:29], v[130:131], v[142:143], v[28:29] op_sel_hi:[0,1,1]
	v_pk_fma_f32 v[26:27], v[130:131], v[140:141], v[26:27] op_sel_hi:[0,1,1]
	v_pk_fma_f32 v[24:25], v[130:131], v[138:139], v[24:25] op_sel_hi:[0,1,1]
	v_pk_fma_f32 v[22:23], v[130:131], v[136:137], v[22:23] op_sel_hi:[0,1,1]
	v_pk_fma_f32 v[20:21], v[130:131], v[134:135], v[20:21] op_sel_hi:[0,1,1]
	v_pk_fma_f32 v[18:19], v[130:131], v[132:133], v[18:19] op_sel_hi:[0,1,1]
.LBB1_17:
	s_cmp_eq_u32 s18, 41
	s_cbranch_scc0 .Lnf_9b
	s_mov_b64 s[14:15], -1
	s_and_b64 s[20:21], s[6:7], s[14:15]
	s_and_saveexec_b64 s[14:15], s[20:21]
	s_cbranch_execz .LBB1_9
	v_cvt_pk_f16_f32 v133, v8, v9
	v_cvt_pk_f16_f32 v132, v6, v7
	v_cvt_pk_f16_f32 v131, v4, v5
	v_cvt_pk_f16_f32 v130, v2, v3
	ds_write_b128 v223, v[130:133]
	v_cvt_pk_f16_f32 v133, v16, v17
	v_cvt_pk_f16_f32 v132, v14, v15
	v_cvt_pk_f16_f32 v131, v12, v13
	v_cvt_pk_f16_f32 v130, v10, v11
	ds_write_b128 v223, v[130:133] offset:1024
	v_cvt_pk_f16_f32 v133, v56, v57
	v_cvt_pk_f16_f32 v132, v54, v55
	v_cvt_pk_f16_f32 v131, v52, v53
	v_cvt_pk_f16_f32 v130, v50, v51
	ds_write_b128 v223, v[130:133] offset:2048
	v_cvt_pk_f16_f32 v133, v64, v65
	v_cvt_pk_f16_f32 v132, v62, v63
	v_cvt_pk_f16_f32 v131, v60, v61
	v_cvt_pk_f16_f32 v130, v58, v59
	ds_write_b128 v223, v[130:133] offset:3072
	v_cvt_pk_f16_f32 v133, v40, v41
	v_cvt_pk_f16_f32 v132, v38, v39
	v_cvt_pk_f16_f32 v131, v36, v37
	v_cvt_pk_f16_f32 v130, v34, v35
	ds_write_b128 v223, v[130:133] offset:4096
	v_cvt_pk_f16_f32 v133, v48, v49
	v_cvt_pk_f16_f32 v132, v46, v47
	v_cvt_pk_f16_f32 v131, v44, v45
	v_cvt_pk_f16_f32 v130, v42, v43
	ds_write_b128 v223, v[130:133] offset:5120
	v_cvt_pk_f16_f32 v133, v24, v25
	v_cvt_pk_f16_f32 v132, v22, v23
	v_cvt_pk_f16_f32 v131, v20, v21
	v_cvt_pk_f16_f32 v130, v18, v19
	ds_write_b128 v223, v[130:133] offset:6144
	v_cvt_pk_f16_f32 v133, v32, v33
	v_cvt_pk_f16_f32 v132, v30, v31
	v_cvt_pk_f16_f32 v131, v28, v29
	v_cvt_pk_f16_f32 v130, v26, v27
	ds_write_b128 v223, v[130:133] offset:7168
	s_branch .LBB1_9
.Lnf_inact:
	s_add_u32 s22, s12, 0x12000
	v_readfirstlane_b32 s19, v0
	s_addc_u32 s23, s16, 0
	s_lshl_b32 s19, s19, 4
	s_and_b32 s21, s19, 0xfffffc00
	s_add_i32 s21, s21, s26
	s_cmp_lg_u32 s3, -1
	s_cselect_b32 s24, s3, 0
	s_add_i32 s21, s21, s24
	s_mov_b32 m0, s21
	s_nop 0
	global_load_lds_dwordx4 v226, s[22:23]
	s_add_u32 s22, s12, 0x14000
	s_addc_u32 s23, s16, 0
	s_add_i32 s24, s21, 0x2000
	s_mov_b32 m0, s24
	s_nop 0
	global_load_lds_dwordx4 v226, s[22:23]
	s_add_u32 s22, s12, 0x16000
	s_addc_u32 s23, s16, 0
	s_add_i32 s24, s21, 0x4000
	s_mov_b32 m0, s24
	s_nop 0
	global_load_lds_dwordx4 v226, s[22:23]
	s_add_u32 s22, s12, 0x18000
	s_addc_u32 s23, s16, 0
	s_add_i32 s24, s21, 0x6000
	s_mov_b32 m0, s24
	s_nop 0
	global_load_lds_dwordx4 v226, s[22:23]
	s_add_u32 s22, s12, 0x1a000
	s_addc_u32 s23, s16, 0
	s_and_b32 s19, s19, 0xfffff000
	s_sub_i32 s19, s21, s19
	s_add_i32 s19, s19, 0x8000
	s_mov_b32 m0, s19
	s_nop 0
	global_load_lds_dwordx4 v224, s[22:23]
	s_branch .LBB1_17
.LBB1_19:
	s_lshr_b32 s33, s25, 15
	s_and_saveexec_b64 s[14:15], s[4:5]
	s_cbranch_execz .LBB1_21
	ds_read_b128 v[66:69], v223
	ds_read_b128 v[70:73], v223 offset:1024
	s_waitcnt lgkmcnt(1)
	v_cvt_f32_f16_sdwa v75, v66 dst_sel:DWORD dst_unused:UNUSED_PAD src0_sel:WORD_1
	v_cvt_f32_f16_e32 v74, v66
	v_cvt_f32_f16_sdwa v77, v67 dst_sel:DWORD dst_unused:UNUSED_PAD src0_sel:WORD_1
	v_cvt_f32_f16_e32 v76, v67
	v_cvt_f32_f16_sdwa v67, v68 dst_sel:DWORD dst_unused:UNUSED_PAD src0_sel:WORD_1
	v_pk_add_f32 v[2:3], v[2:3], v[74:75]
	v_cvt_f32_f16_e32 v66, v68
	v_cvt_pk_f16_f32 v146, v2, v3
	v_cvt_f32_f16_sdwa v3, v69 dst_sel:DWORD dst_unused:UNUSED_PAD src0_sel:WORD_1
	v_cvt_f32_f16_e32 v2, v69
	v_pk_add_f32 v[4:5], v[4:5], v[76:77]
	v_pk_add_f32 v[2:3], v[8:9], v[2:3]
	v_cvt_pk_f16_f32 v147, v4, v5
	v_pk_add_f32 v[4:5], v[6:7], v[66:67]
	v_cvt_pk_f16_f32 v149, v2, v3
	s_waitcnt lgkmcnt(0)
	v_cvt_f32_f16_sdwa v3, v70 dst_sel:DWORD dst_unused:UNUSED_PAD src0_sel:WORD_1
	v_cvt_f32_f16_e32 v2, v70
	v_cvt_pk_f16_f32 v148, v4, v5
	v_cvt_f32_f16_sdwa v5, v71 dst_sel:DWORD dst_unused:UNUSED_PAD src0_sel:WORD_1
	v_cvt_f32_f16_e32 v4, v71
	v_pk_add_f32 v[2:3], v[10:11], v[2:3]
	v_cvt_f32_f16_sdwa v7, v73 dst_sel:DWORD dst_unused:UNUSED_PAD src0_sel:WORD_1
	v_cvt_pk_f16_f32 v150, v2, v3
	v_pk_add_f32 v[2:3], v[12:13], v[4:5]
	v_cvt_f32_f16_sdwa v5, v72 dst_sel:DWORD dst_unused:UNUSED_PAD src0_sel:WORD_1
	v_cvt_f32_f16_e32 v4, v72
	v_cvt_pk_f16_f32 v151, v2, v3
	v_cvt_f32_f16_e32 v6, v73
	ds_write_b128 v223, v[146:149]
	v_pk_add_f32 v[8:9], v[14:15], v[4:5]
	ds_read_b128 v[2:5], v223 offset:2048
	v_pk_add_f32 v[6:7], v[16:17], v[6:7]
	v_cvt_pk_f16_f32 v152, v8, v9
	v_cvt_pk_f16_f32 v153, v6, v7
	ds_read_b128 v[6:9], v223 offset:3072
	s_waitcnt lgkmcnt(1)
	v_cvt_f32_f16_sdwa v11, v2 dst_sel:DWORD dst_unused:UNUSED_PAD src0_sel:WORD_1
	v_cvt_f32_f16_e32 v10, v2
	v_cvt_f32_f16_sdwa v13, v3 dst_sel:DWORD dst_unused:UNUSED_PAD src0_sel:WORD_1
	v_cvt_f32_f16_e32 v12, v3
	ds_write_b128 v223, v[150:153] offset:1024
	v_pk_add_f32 v[2:3], v[50:51], v[10:11]
	v_cvt_f32_f16_sdwa v11, v4 dst_sel:DWORD dst_unused:UNUSED_PAD src0_sel:WORD_1
	v_cvt_f32_f16_e32 v10, v4
	v_cvt_pk_f16_f32 v154, v2, v3
	v_pk_add_f32 v[2:3], v[52:53], v[12:13]
	v_cvt_f32_f16_sdwa v13, v5 dst_sel:DWORD dst_unused:UNUSED_PAD src0_sel:WORD_1
	v_cvt_f32_f16_e32 v12, v5
	v_cvt_pk_f16_f32 v155, v2, v3
	v_pk_add_f32 v[2:3], v[54:55], v[10:11]
	s_waitcnt lgkmcnt(1)
	v_cvt_f32_f16_sdwa v5, v7 dst_sel:DWORD dst_unused:UNUSED_PAD src0_sel:WORD_1
	v_cvt_pk_f16_f32 v156, v2, v3
	v_pk_add_f32 v[2:3], v[56:57], v[12:13]
	v_cvt_f32_f16_e32 v4, v7
	v_cvt_pk_f16_f32 v157, v2, v3
	v_cvt_f32_f16_sdwa v3, v6 dst_sel:DWORD dst_unused:UNUSED_PAD src0_sel:WORD_1
	v_cvt_f32_f16_e32 v2, v6
	v_cvt_f32_f16_sdwa v7, v9 dst_sel:DWORD dst_unused:UNUSED_PAD src0_sel:WORD_1
	v_cvt_f32_f16_e32 v6, v9
	ds_write_b128 v223, v[154:157] offset:2048
	v_pk_add_f32 v[2:3], v[58:59], v[2:3]
	v_pk_add_f32 v[6:7], v[64:65], v[6:7]
	v_cvt_pk_f16_f32 v158, v2, v3
	v_pk_add_f32 v[2:3], v[60:61], v[4:5]
	v_cvt_f32_f16_sdwa v5, v8 dst_sel:DWORD dst_unused:UNUSED_PAD src0_sel:WORD_1
	v_cvt_f32_f16_e32 v4, v8
	v_cvt_pk_f16_f32 v159, v2, v3
	v_cvt_pk_f16_f32 v161, v6, v7
	v_pk_add_f32 v[8:9], v[62:63], v[4:5]
	ds_read_b128 v[2:5], v223 offset:4096
	v_cvt_pk_f16_f32 v160, v8, v9
	ds_read_b128 v[6:9], v223 offset:5120
	ds_write_b128 v223, v[158:161] offset:3072
	s_waitcnt lgkmcnt(2)
	v_cvt_f32_f16_sdwa v11, v2 dst_sel:DWORD dst_unused:UNUSED_PAD src0_sel:WORD_1
	v_cvt_f32_f16_e32 v10, v2
	v_cvt_f32_f16_sdwa v13, v3 dst_sel:DWORD dst_unused:UNUSED_PAD src0_sel:WORD_1
	v_cvt_f32_f16_e32 v12, v3
	v_pk_add_f32 v[2:3], v[34:35], v[10:11]
	v_cvt_f32_f16_sdwa v11, v4 dst_sel:DWORD dst_unused:UNUSED_PAD src0_sel:WORD_1
	v_cvt_f32_f16_e32 v10, v4
	v_cvt_pk_f16_f32 v162, v2, v3
	v_pk_add_f32 v[2:3], v[36:37], v[12:13]
	v_cvt_f32_f16_sdwa v13, v5 dst_sel:DWORD dst_unused:UNUSED_PAD src0_sel:WORD_1
	v_cvt_f32_f16_e32 v12, v5
	v_cvt_pk_f16_f32 v163, v2, v3
	v_pk_add_f32 v[2:3], v[38:39], v[10:11]
	s_waitcnt lgkmcnt(1)
	v_cvt_f32_f16_sdwa v5, v7 dst_sel:DWORD dst_unused:UNUSED_PAD src0_sel:WORD_1
	v_cvt_pk_f16_f32 v164, v2, v3
	v_pk_add_f32 v[2:3], v[40:41], v[12:13]
	v_cvt_f32_f16_e32 v4, v7
	v_cvt_pk_f16_f32 v165, v2, v3
	v_cvt_f32_f16_sdwa v3, v6 dst_sel:DWORD dst_unused:UNUSED_PAD src0_sel:WORD_1
	v_cvt_f32_f16_e32 v2, v6
	v_cvt_f32_f16_sdwa v7, v9 dst_sel:DWORD dst_unused:UNUSED_PAD src0_sel:WORD_1
	v_cvt_f32_f16_e32 v6, v9
	ds_write_b128 v223, v[162:165] offset:4096
	v_pk_add_f32 v[2:3], v[42:43], v[2:3]
	v_pk_add_f32 v[6:7], v[48:49], v[6:7]
	v_cvt_pk_f16_f32 v166, v2, v3
	v_pk_add_f32 v[2:3], v[44:45], v[4:5]
	v_cvt_f32_f16_sdwa v5, v8 dst_sel:DWORD dst_unused:UNUSED_PAD src0_sel:WORD_1
	v_cvt_f32_f16_e32 v4, v8
	v_cvt_pk_f16_f32 v167, v2, v3
	v_cvt_pk_f16_f32 v169, v6, v7
	v_pk_add_f32 v[8:9], v[46:47], v[4:5]
	ds_read_b128 v[2:5], v223 offset:6144
	v_cvt_pk_f16_f32 v168, v8, v9
	ds_read_b128 v[6:9], v223 offset:7168
	ds_write_b128 v223, v[166:169] offset:5120
	s_waitcnt lgkmcnt(2)
	v_cvt_f32_f16_sdwa v11, v2 dst_sel:DWORD dst_unused:UNUSED_PAD src0_sel:WORD_1
	v_cvt_f32_f16_e32 v10, v2
	v_cvt_f32_f16_sdwa v13, v3 dst_sel:DWORD dst_unused:UNUSED_PAD src0_sel:WORD_1
	v_cvt_f32_f16_e32 v12, v3
	v_pk_add_f32 v[2:3], v[18:19], v[10:11]
	v_cvt_f32_f16_sdwa v11, v4 dst_sel:DWORD dst_unused:UNUSED_PAD src0_sel:WORD_1
	v_cvt_f32_f16_e32 v10, v4
	v_cvt_pk_f16_f32 v170, v2, v3
	v_pk_add_f32 v[2:3], v[20:21], v[12:13]
	v_cvt_f32_f16_sdwa v13, v5 dst_sel:DWORD dst_unused:UNUSED_PAD src0_sel:WORD_1
	v_cvt_f32_f16_e32 v12, v5
	v_cvt_pk_f16_f32 v171, v2, v3
	v_pk_add_f32 v[2:3], v[22:23], v[10:11]
	s_waitcnt lgkmcnt(1)
	v_cvt_f32_f16_sdwa v5, v7 dst_sel:DWORD dst_unused:UNUSED_PAD src0_sel:WORD_1
	v_cvt_pk_f16_f32 v172, v2, v3
	v_pk_add_f32 v[2:3], v[24:25], v[12:13]
	v_cvt_f32_f16_e32 v4, v7
	v_cvt_pk_f16_f32 v173, v2, v3
	v_cvt_f32_f16_sdwa v3, v6 dst_sel:DWORD dst_unused:UNUSED_PAD src0_sel:WORD_1
	v_cvt_f32_f16_e32 v2, v6
	v_cvt_f32_f16_sdwa v7, v9 dst_sel:DWORD dst_unused:UNUSED_PAD src0_sel:WORD_1
	v_cvt_f32_f16_e32 v6, v9
	ds_write_b128 v223, v[170:173] offset:6144
	v_pk_add_f32 v[2:3], v[26:27], v[2:3]
	s_nop 0
	v_cvt_pk_f16_f32 v174, v2, v3
	v_pk_add_f32 v[2:3], v[28:29], v[4:5]
	v_cvt_f32_f16_sdwa v5, v8 dst_sel:DWORD dst_unused:UNUSED_PAD src0_sel:WORD_1
	v_cvt_f32_f16_e32 v4, v8
	v_cvt_pk_f16_f32 v175, v2, v3
	v_pk_add_f32 v[2:3], v[30:31], v[4:5]
	s_nop 0
	v_cvt_pk_f16_f32 v176, v2, v3
	v_pk_add_f32 v[2:3], v[32:33], v[6:7]
	s_nop 0
	v_cvt_pk_f16_f32 v177, v2, v3
	ds_write_b128 v223, v[174:177] offset:7168

.LBB1_33:
	s_or_b64 exec, exec, s[16:17]
	s_and_b32 s16, s40, 7
.Lfin_33b:
	s_mul_i32 s18, s33, 0x9000
	s_add_i32 s19, s18, 0x8000
	s_cmp_lg_u32 s16, 0
	v_add_u32_e32 v231, s19, v246
	s_cbranch_scc1 .LBB1_35
	ds_read_b128 v[2:5], v231 offset:33280
	ds_read_b128 v[6:9], v231 offset:33312
	ds_read_b128 v[10:13], v231 offset:33344
	ds_read_b128 v[14:17], v231 offset:33376
	ds_read_b128 v[18:21], v231 offset:33408
	ds_read_b128 v[22:25], v231 offset:33440
	ds_read_b128 v[26:29], v231 offset:33472
	ds_read_b128 v[30:33], v231 offset:33504
	ds_read_b128 v[34:37], v231 offset:33536
	ds_read_b128 v[38:41], v231 offset:33568
	ds_read_b128 v[42:45], v231 offset:33600
	ds_read_b128 v[46:49], v231 offset:33632
	ds_read_b128 v[50:53], v231 offset:33664
	ds_read_b128 v[54:57], v231 offset:33696
	ds_read_b128 v[58:61], v231 offset:33728
	ds_read_b128 v[62:65], v231 offset:33760
	s_waitcnt lgkmcnt(12)
	v_mfma_f32_32x32x16_f16 v[2:17], v[178:181], v[146:149], v[2:17]
	s_waitcnt lgkmcnt(8)
	v_mfma_f32_32x32x16_f16 v[18:33], v[178:181], v[154:157], v[18:33]
	s_waitcnt lgkmcnt(4)
	v_mfma_f32_32x32x16_f16 v[34:49], v[178:181], v[162:165], v[34:49]
	s_waitcnt lgkmcnt(0)
	v_mfma_f32_32x32x16_f16 v[50:65], v[178:181], v[170:173], v[50:65]
	v_mfma_f32_32x32x16_f16 v[2:17], v[182:185], v[150:153], v[2:17]
	v_mfma_f32_32x32x16_f16 v[18:33], v[182:185], v[158:161], v[18:33]
	v_mfma_f32_32x32x16_f16 v[34:49], v[182:185], v[166:169], v[34:49]
	v_mfma_f32_32x32x16_f16 v[50:65], v[182:185], v[174:177], v[50:65]
.LBB1_35:
	v_add_u32_e32 v82, s18, v247
	ds_read_b128 v[66:69], v231 offset:32768
	ds_read_b128 v[70:73], v231 offset:32800
	ds_read_b128 v[74:77], v231 offset:32832
	ds_read_b128 v[78:81], v231 offset:32864
	ds_read_b128 v[190:193], v82 offset:32768
	ds_read_b128 v[194:197], v82 offset:33792
	ds_read_b128 v[198:201], v82 offset:34816
	ds_read_b128 v[202:205], v82 offset:35840
	ds_read_b128 v[212:215], v82 offset:36864
	ds_read_b128 v[232:235], v82 offset:37888
	ds_read_b128 v[236:239], v82 offset:38912
	ds_read_b128 v[240:243], v82 offset:39936
	s_waitcnt lgkmcnt(7)
	v_mfma_f32_32x32x16_f16 v[66:81], v[190:193], v[146:149], v[66:81]
	s_add_i32 s17, s18, 0xffff7000
	s_cmp_lg_u32 s33, 0
	s_cselect_b32 s17, s17, 0x12000
	s_waitcnt lgkmcnt(6)
	v_mfma_f32_32x32x16_f16 v[66:81], v[194:197], v[150:153], v[66:81]
	s_waitcnt lgkmcnt(5)
	v_mfma_f32_32x32x16_f16 v[66:81], v[198:201], v[154:157], v[66:81]
	s_waitcnt lgkmcnt(4)
	v_mfma_f32_32x32x16_f16 v[66:81], v[202:205], v[158:161], v[66:81]
	v_readfirstlane_b32 s18, v0
	s_lshl_b32 s20, s18, 4
	s_and_b32 s18, s20, 0xfffffc00
	s_add_i32 s17, s18, s17
	s_cmp_lg_u32 s3, -1
	s_cselect_b32 s18, s3, 0
	s_add_i32 s17, s17, s18
	s_add_u32 s18, s14, 0x372000
	s_addc_u32 s19, s15, 0
	s_mov_b32 m0, s17
	s_nop 0
	global_load_lds_dwordx4 v226, s[18:19]
	s_waitcnt lgkmcnt(3)
	v_mfma_f32_32x32x16_f16 v[66:81], v[212:215], v[162:165], v[66:81]
	s_add_u32 s18, s14, 0x374000
	s_addc_u32 s19, s15, 0
	s_add_i32 s21, s17, 0x2000
	s_mov_b32 m0, s21
	s_nop 0
	global_load_lds_dwordx4 v226, s[18:19]
	s_waitcnt lgkmcnt(2)
	v_mfma_f32_32x32x16_f16 v[66:81], v[232:235], v[166:169], v[66:81]
	s_add_u32 s18, s14, 0x376000
	s_addc_u32 s19, s15, 0
	s_add_i32 s21, s17, 0x4000
	s_mov_b32 m0, s21
	s_nop 0
	global_load_lds_dwordx4 v226, s[18:19]
	s_waitcnt lgkmcnt(1)
	v_mfma_f32_32x32x16_f16 v[66:81], v[236:239], v[170:173], v[66:81]
	s_add_u32 s18, s14, 0x378000
	s_addc_u32 s19, s15, 0
	s_add_i32 s21, s17, 0x6000
	s_mov_b32 m0, s21
	s_nop 0
	global_load_lds_dwordx4 v226, s[18:19]
	s_waitcnt lgkmcnt(0)
	v_mfma_f32_32x32x16_f16 v[66:81], v[240:243], v[174:177], v[66:81]
	s_add_u32 s18, s14, 0x37a000
	s_addc_u32 s19, s15, 0
	s_and_b32 s20, s20, 0xfffff000
	s_sub_i32 s17, s17, s20
	s_add_i32 s17, s17, 0x8000
	s_mov_b32 m0, s17
	s_nop 0
	global_load_lds_dwordx4 v224, s[18:19]
	ds_read_b128 v[190:193], v82 offset:40960
	ds_read_b128 v[194:197], v82 offset:41984
	ds_read_b128 v[198:201], v82 offset:43008
	ds_read_b128 v[202:205], v82 offset:44032
	ds_read_b128 v[212:215], v82 offset:45056
	ds_read_b128 v[232:235], v82 offset:46080
	ds_read_b128 v[236:239], v82 offset:47104
	ds_read_b128 v[240:243], v82 offset:48128
	v_cvt_pk_f16_f32 v66, v66, v67
	v_cvt_pk_f16_f32 v67, v68, v69
	v_cvt_pk_f16_f32 v68, v70, v71
	v_cvt_pk_f16_f32 v69, v72, v73
	v_and_b32_e32 v70, 0x7fff7fff, v66
	v_and_b32_e32 v71, 0x7fff7fff, v67
	v_and_b32_e32 v72, 0x7fff7fff, v68
	v_and_b32_e32 v73, 0x7fff7fff, v69
	v_pk_min_f16 v70, v70, v229
	v_pk_min_f16 v71, v71, v229
	v_pk_min_f16 v72, v72, v229
	v_pk_min_f16 v73, v73, v229
	v_pk_max_f16 v66, v66, v228
	v_pk_max_f16 v67, v67, v228
	s_nop 0
	v_pk_fma_f16 v70, v70, s26, -1.0 op_sel_hi:[1,0,0]
	v_pk_fma_f16 v71, v71, s26, -1.0 op_sel_hi:[1,0,0]
	v_pk_fma_f16 v72, v72, s26, -1.0 op_sel_hi:[1,0,0]
	v_pk_fma_f16 v73, v73, s26, -1.0 op_sel_hi:[1,0,0]
	v_pk_fma_f16 v82, v70, s27, v230 op_sel_hi:[1,0,0]
	v_pk_fma_f16 v83, v71, s27, v230 op_sel_hi:[1,0,0]
	v_pk_fma_f16 v144, v72, s27, v230 op_sel_hi:[1,0,0]
	v_pk_fma_f16 v145, v73, s27, v230 op_sel_hi:[1,0,0]
	v_pk_fma_f16 v82, v70, v82, s28 op_sel_hi:[1,1,0]
	v_pk_fma_f16 v83, v71, v83, s28 op_sel_hi:[1,1,0]
	v_pk_fma_f16 v144, v72, v144, s28 op_sel_hi:[1,1,0]
	v_pk_fma_f16 v145, v73, v145, s28 op_sel_hi:[1,1,0]
	v_pk_fma_f16 v82, v70, v82, s29 op_sel_hi:[1,1,0]
	v_pk_fma_f16 v83, v71, v83, s29 op_sel_hi:[1,1,0]
	v_pk_fma_f16 v144, v72, v144, s29 op_sel_hi:[1,1,0]
	v_pk_fma_f16 v145, v73, v145, s29 op_sel_hi:[1,1,0]
	v_pk_fma_f16 v82, v70, v82, s30 op_sel_hi:[1,1,0]
	v_pk_fma_f16 v83, v71, v83, s30 op_sel_hi:[1,1,0]
	v_pk_fma_f16 v144, v72, v144, s30 op_sel_hi:[1,1,0]
	v_pk_fma_f16 v145, v73, v145, s30 op_sel_hi:[1,1,0]
	v_pk_fma_f16 v82, v70, v82, s31 op_sel_hi:[1,1,0]
	v_pk_fma_f16 v83, v71, v83, s31 op_sel_hi:[1,1,0]
	v_pk_fma_f16 v144, v72, v144, s31 op_sel_hi:[1,1,0]
	v_pk_fma_f16 v145, v73, v145, s31 op_sel_hi:[1,1,0]
	v_pk_fma_f16 v82, v70, v82, s41 op_sel_hi:[1,1,0]
	v_pk_fma_f16 v83, v71, v83, s41 op_sel_hi:[1,1,0]
	v_pk_fma_f16 v144, v72, v144, s41 op_sel_hi:[1,1,0]
	v_pk_fma_f16 v145, v73, v145, s41 op_sel_hi:[1,1,0]
	v_pk_max_f16 v68, v68, v228
	v_pk_max_f16 v69, v69, v228
	v_pk_fma_f16 v70, v70, v82, s42 op_sel_hi:[1,1,0]
	v_pk_fma_f16 v71, v71, v83, s42 op_sel_hi:[1,1,0]
	v_pk_fma_f16 v72, v72, v144, s42 op_sel_hi:[1,1,0]
	v_pk_fma_f16 v73, v73, v145, s42 op_sel_hi:[1,1,0]
	v_pk_add_f16 v66, v66, v70
	v_pk_add_f16 v67, v67, v71
	v_pk_add_f16 v68, v68, v72
	v_pk_add_f16 v69, v69, v73
	v_cvt_pk_f16_f32 v70, v74, v75
	v_cvt_pk_f16_f32 v71, v76, v77
	v_cvt_pk_f16_f32 v72, v78, v79
	v_cvt_pk_f16_f32 v73, v80, v81
	v_and_b32_e32 v74, 0x7fff7fff, v70
	v_and_b32_e32 v75, 0x7fff7fff, v71
	v_and_b32_e32 v76, 0x7fff7fff, v72
	v_and_b32_e32 v77, 0x7fff7fff, v73
	v_pk_min_f16 v74, v74, v229
	v_pk_min_f16 v75, v75, v229
	v_pk_min_f16 v76, v76, v229
	v_pk_min_f16 v77, v77, v229
	s_waitcnt lgkmcnt(7)
	v_mfma_f32_32x32x16_f16 v[2:17], v[190:193], v[66:69], v[2:17]
	v_pk_fma_f16 v74, v74, s26, -1.0 op_sel_hi:[1,0,0]
	v_pk_fma_f16 v75, v75, s26, -1.0 op_sel_hi:[1,0,0]
	v_pk_fma_f16 v76, v76, s26, -1.0 op_sel_hi:[1,0,0]
	v_pk_fma_f16 v77, v77, s26, -1.0 op_sel_hi:[1,0,0]
	v_pk_fma_f16 v78, v74, s27, v230 op_sel_hi:[1,0,0]
	v_pk_fma_f16 v79, v75, s27, v230 op_sel_hi:[1,0,0]
	v_pk_fma_f16 v80, v76, s27, v230 op_sel_hi:[1,0,0]
	v_pk_fma_f16 v81, v77, s27, v230 op_sel_hi:[1,0,0]
	s_waitcnt lgkmcnt(5)
	v_mfma_f32_32x32x16_f16 v[18:33], v[198:201], v[66:69], v[18:33]
	v_pk_fma_f16 v78, v74, v78, s28 op_sel_hi:[1,1,0]
	v_pk_fma_f16 v79, v75, v79, s28 op_sel_hi:[1,1,0]
	v_pk_fma_f16 v80, v76, v80, s28 op_sel_hi:[1,1,0]
	v_pk_fma_f16 v81, v77, v81, s28 op_sel_hi:[1,1,0]
	v_pk_fma_f16 v78, v74, v78, s29 op_sel_hi:[1,1,0]
	v_pk_fma_f16 v79, v75, v79, s29 op_sel_hi:[1,1,0]
	v_pk_fma_f16 v80, v76, v80, s29 op_sel_hi:[1,1,0]
	s_waitcnt lgkmcnt(3)
	v_mfma_f32_32x32x16_f16 v[34:49], v[212:215], v[66:69], v[34:49]
	v_pk_fma_f16 v81, v77, v81, s29 op_sel_hi:[1,1,0]
	v_pk_fma_f16 v78, v74, v78, s30 op_sel_hi:[1,1,0]
	v_pk_fma_f16 v79, v75, v79, s30 op_sel_hi:[1,1,0]
	v_pk_fma_f16 v80, v76, v80, s30 op_sel_hi:[1,1,0]
	v_pk_fma_f16 v81, v77, v81, s30 op_sel_hi:[1,1,0]
	v_pk_fma_f16 v78, v74, v78, s31 op_sel_hi:[1,1,0]
	v_pk_fma_f16 v79, v75, v79, s31 op_sel_hi:[1,1,0]
	s_waitcnt lgkmcnt(1)
	v_mfma_f32_32x32x16_f16 v[50:65], v[236:239], v[66:69], v[50:65]
	v_pk_fma_f16 v80, v76, v80, s31 op_sel_hi:[1,1,0]
	v_pk_fma_f16 v81, v77, v81, s31 op_sel_hi:[1,1,0]
	v_pk_fma_f16 v78, v74, v78, s41 op_sel_hi:[1,1,0]
	v_pk_fma_f16 v79, v75, v79, s41 op_sel_hi:[1,1,0]
	v_pk_fma_f16 v80, v76, v80, s41 op_sel_hi:[1,1,0]
	v_pk_fma_f16 v81, v77, v81, s41 op_sel_hi:[1,1,0]
	v_pk_max_f16 v70, v70, v228
	v_pk_max_f16 v71, v71, v228
	v_pk_max_f16 v72, v72, v228
	v_pk_max_f16 v73, v73, v228
	v_pk_fma_f16 v74, v74, v78, s42 op_sel_hi:[1,1,0]
	v_pk_fma_f16 v75, v75, v79, s42 op_sel_hi:[1,1,0]
	v_pk_fma_f16 v76, v76, v80, s42 op_sel_hi:[1,1,0]
	v_pk_fma_f16 v77, v77, v81, s42 op_sel_hi:[1,1,0]
	v_pk_add_f16 v70, v70, v74
	v_pk_add_f16 v71, v71, v75
	v_pk_add_f16 v72, v72, v76
	v_pk_add_f16 v73, v73, v77
	s_cmp_lg_u32 s16, 7
	s_nop 0
	v_mfma_f32_32x32x16_f16 v[2:17], v[194:197], v[70:73], v[2:17]
	v_mfma_f32_32x32x16_f16 v[18:33], v[202:205], v[70:73], v[18:33]
	v_mfma_f32_32x32x16_f16 v[34:49], v[232:235], v[70:73], v[34:49]
	s_waitcnt lgkmcnt(0)
	v_mfma_f32_32x32x16_f16 v[50:65], v[240:243], v[70:73], v[50:65]
	s_cbranch_scc1 .LBB1_25
	ds_read_b128 v[198:201], v231 offset:33280
	ds_read_b128 v[190:193], v231 offset:33312
	ds_read_b128 v[202:205], v231 offset:33792
	ds_read_b128 v[194:197], v231 offset:33824
	ds_read_b128 v[74:77], v231 offset:33344
	ds_read_b128 v[66:69], v231 offset:33376
	ds_read_b128 v[78:81], v231 offset:33856
	ds_read_b128 v[70:73], v231 offset:33888
	s_lshr_b32 s24, s40, 3
	s_cmp_lt_u32 s40, 16
	s_cselect_b64 s[16:17], -1, 0
	s_cmp_gt_u32 s40, 15
	s_cselect_b64 s[22:23], -1, 0
	s_and_saveexec_b64 s[18:19], s[8:9]
	s_xor_b64 s[18:19], exec, s[18:19]
	s_cbranch_execz .LBB1_41
	s_mov_b64 s[20:21], -1
	s_and_b64 vcc, exec, s[22:23]
	s_cbranch_vccz .LBB1_39
	s_cmp_eq_u32 s24, 2
	s_cselect_b32 s25, 2, -1
	s_mov_b64 s[20:21], 0

	.amdhsa_kernel _Z10ple_kernelPKfPKDv8_DF16_PKcS0_S0_S0_S0_S0_S0_Pf
		.amdhsa_group_segment_fixed_size 0
		.amdhsa_private_segment_fixed_size 0
		.amdhsa_kernarg_size 80
		.amdhsa_user_sgpr_count 2
		.amdhsa_user_sgpr_dispatch_ptr 0
		.amdhsa_user_sgpr_queue_ptr 0
		.amdhsa_user_sgpr_kernarg_segment_ptr 1
		.amdhsa_user_sgpr_dispatch_id 0
		.amdhsa_user_sgpr_kernarg_preload_length 0
		.amdhsa_user_sgpr_kernarg_preload_offset 0
		.amdhsa_user_sgpr_private_segment_size 0
		.amdhsa_uses_dynamic_stack 0
		.amdhsa_enable_private_segment 0
		.amdhsa_system_sgpr_workgroup_id_x 1
		.amdhsa_system_sgpr_workgroup_id_y 0
		.amdhsa_system_sgpr_workgroup_id_z 0
		.amdhsa_system_sgpr_workgroup_info 0
		.amdhsa_system_vgpr_workitem_id 0
		.amdhsa_next_free_vgpr 248
		.amdhsa_next_free_sgpr 63
		.amdhsa_accum_offset 248
		.amdhsa_reserve_vcc 1
		.amdhsa_float_round_mode_32 0
		.amdhsa_float_round_mode_16_64 0
		.amdhsa_float_denorm_mode_32 3
		.amdhsa_float_denorm_mode_16_64 3
		.amdhsa_dx10_clamp 1
		.amdhsa_ieee_mode 1
		.amdhsa_fp16_overflow 0
		.amdhsa_tg_split 0
		.amdhsa_exception_fp_ieee_invalid_op 0
		.amdhsa_exception_fp_denorm_src 0
		.amdhsa_exception_fp_ieee_div_zero 0
		.amdhsa_exception_fp_ieee_overflow 0
		.amdhsa_exception_fp_ieee_underflow 0
		.amdhsa_exception_fp_ieee_inexact 0
		.amdhsa_exception_int_div_zero 0
	.end_amdhsa_kernel

amdhsa.kernels:
  - .agpr_count:     0
    .args:
      - .actual_access:  read_only
        .address_space:  global
        .offset:         0
        .size:           8
        .value_kind:     global_buffer
      - .actual_access:  read_only
        .address_space:  global
        .offset:         8
        .size:           8
        .value_kind:     global_buffer
      - .actual_access:  read_only
        .address_space:  global
        .offset:         16
        .size:           8
        .value_kind:     global_buffer
      - .actual_access:  read_only
        .address_space:  global
        .offset:         24
        .size:           8
        .value_kind:     global_buffer
      - .actual_access:  read_only
        .address_space:  global
        .offset:         32
        .size:           8
        .value_kind:     global_buffer
      - .actual_access:  read_only
        .address_space:  global
        .offset:         40
        .size:           8
        .value_kind:     global_buffer
      - .actual_access:  read_only
        .address_space:  global
        .offset:         48
        .size:           8
        .value_kind:     global_buffer
      - .actual_access:  read_only
        .address_space:  global
        .offset:         56
        .size:           8
        .value_kind:     global_buffer
      - .actual_access:  read_only
        .address_space:  global
        .offset:         64
        .size:           8
        .value_kind:     global_buffer
      - .actual_access:  read_only
        .address_space:  global
        .offset:         72
        .size:           8
        .value_kind:     global_buffer
      - .actual_access:  write_only
        .address_space:  global
        .offset:         80
        .size:           8
        .value_kind:     global_buffer
      - .actual_access:  write_only
        .address_space:  global
        .offset:         88
        .size:           8
        .value_kind:     global_buffer
    .group_segment_fixed_size: 0
    .kernarg_segment_align: 8
    .kernarg_segment_size: 96
    .language:       OpenCL C
    .language_version:
      - 2
      - 0
    .max_flat_workgroup_size: 1024
    .name:           _Z11prep_kernelPKfS0_S0_S0_S0_S0_S0_S0_S0_S0_PDv8_DF16_S2_
    .private_segment_fixed_size: 0
    .sgpr_count:     34
    .sgpr_spill_count: 0
    .symbol:         _Z11prep_kernelPKfS0_S0_S0_S0_S0_S0_S0_S0_S0_PDv8_DF16_S2_.kd
    .uniform_work_group_size: 1
    .uses_dynamic_stack: false
    .vgpr_count:     23
    .vgpr_spill_count: 0
    .wavefront_size: 64
  - .agpr_count:     0
    .args:
      - .actual_access:  read_only
        .address_space:  global
        .offset:         0
        .size:           8
        .value_kind:     global_buffer
      - .actual_access:  read_only
        .address_space:  global
        .offset:         8
        .size:           8
        .value_kind:     global_buffer
      - .address_space:  global
        .offset:         16
        .size:           8
        .value_kind:     global_buffer
      - .actual_access:  read_only
        .address_space:  global
        .offset:         24
        .size:           8
        .value_kind:     global_buffer
      - .actual_access:  read_only
        .address_space:  global
        .offset:         32
        .size:           8
        .value_kind:     global_buffer
      - .actual_access:  read_only
        .address_space:  global
        .offset:         40
        .size:           8
        .value_kind:     global_buffer
      - .actual_access:  read_only
        .address_space:  global
        .offset:         48
        .size:           8
        .value_kind:     global_buffer
      - .actual_access:  read_only
        .address_space:  global
        .offset:         56
        .size:           8
        .value_kind:     global_buffer
      - .actual_access:  read_only
        .address_space:  global
        .offset:         64
        .size:           8
        .value_kind:     global_buffer
      - .actual_access:  write_only
        .address_space:  global
        .offset:         72
        .size:           8
        .value_kind:     global_buffer
    .group_segment_fixed_size: 0
    .kernarg_segment_align: 8
    .kernarg_segment_size: 80
    .language:       OpenCL C
    .language_version:
      - 2
      - 0
    .max_flat_workgroup_size: 512
    .name:           _Z10ple_kernelPKfPKDv8_DF16_PKcS0_S0_S0_S0_S0_S0_Pf
    .private_segment_fixed_size: 0
    .sgpr_count:     69
    .sgpr_spill_count: 0
    .symbol:         _Z10ple_kernelPKfPKDv8_DF16_PKcS0_S0_S0_S0_S0_S0_Pf.kd
    .uniform_work_group_size: 1
    .uses_dynamic_stack: false
    .vgpr_count:     248
    .vgpr_spill_count: 0
    .wavefront_size: 64
